# expert weight conversion spread over all barrier slots before each layer's MoE phases (1-2 items per wave per barrier), incl. the barrier after the prologue
# speedup vs baseline: 1.0116x; 1.0050x over previous
.Lcvt_site_11:
	s_mov_b32 s31, 11
	s_branch .Lcvt_post

.Lcvt_go:
	s_mul_i32 s27, s27, 7
	s_add_i32 s27, s27, s25
	s_add_i32 s27, s27, -1
	s_mul_i32 s27, s27, s26
	s_add_i32 s30, s30, s27
	s_mov_b32 s27, s24
	s_mov_b32 s25, 1
	s_branch .Lcvt_item
.Lcvt_lock:
	s_cmp_eq_u32 s31, 11
	s_cbranch_scc0 .Lcvt_lk_a
	s_mov_b32 s27, 0
	s_mov_b32 s24, 0
	s_branch .Lcvt_lk_c
.Lcvt_lk_a:
	s_cmp_ge_u32 s31, 8
	s_cbranch_scc0 .Lcvt_lk_b
	s_cmp_gt_u32 s31, 9
	s_cbranch_scc1 .Lcvt_ret
	s_add_i32 s27, s62, 1
	s_sub_i32 s24, s31, 8
	s_cmp_gt_u32 s27, 3
	s_cbranch_scc1 .Lcvt_ret
	s_branch .Lcvt_lk_c
.Lcvt_lk_b:
	s_mov_b32 s24, -1
	s_cmp_eq_u32 s31, 0
	s_cselect_b32 s24, 0, s24
	s_cmp_eq_u32 s31, 1
	s_cselect_b32 s24, 1, s24
	s_cmp_eq_u32 s31, 2
	s_cselect_b32 s24, 2, s24
	s_cmp_eq_u32 s31, 4
	s_cselect_b32 s24, 3, s24
	s_cmp_eq_u32 s31, 6
	s_cselect_b32 s24, 4, s24
	s_cmp_eq_u32 s31, 7
	s_cselect_b32 s24, 5, s24
	s_cmp_lt_i32 s24, 0
	s_cbranch_scc1 .Lcvt_ret
	s_mov_b32 s27, s62
	s_cmp_eq_u32 s62, 0
	s_cselect_b32 s26, 1, 2
	s_add_i32 s24, s24, s26
.Lcvt_lk_c:
	s_mov_b32 s26, 2743
	s_mov_b32 s4, 19200
	s_cmp_eq_u32 s27, 1
	s_cselect_b32 s26, 1980, s26
	s_cselect_b32 s4, 15840, s4
	s_cmp_eq_u32 s27, 2
	s_cselect_b32 s26, 1980, s26
	s_cselect_b32 s4, 15840, s4
	s_cmp_eq_u32 s27, 3
	s_cselect_b32 s26, 2610, s26
	s_cselect_b32 s4, 20880, s4
	s_mul_i32 s30, s24, s26
	s_add_i32 s24, s30, s26
	s_min_u32 s4, s4, s24
	s_mul_i32 s26, s80, 7
	s_add_i32 s26, s26, s25
	s_add_i32 s26, s26, -1
	s_add_i32 s30, s30, s26
	s_mov_b32 s26, 2
	s_movk_i32 s25, 0x700
.Lcvt_item:
	s_cmp_ge_u32 s30, s4
	s_cbranch_scc1 .Lcvt_ret
	s_mov_b32 s6, s27
	s_mov_b32 s5, s30
	s_cmp_eq_u32 s25, 1
	s_cbranch_scc1 .Lcvt_dec
	s_cmp_eq_u32 s27, 3
	s_cbranch_scc1 .Lcvt_m3
	s_mov_b32 s24, 5376
	s_cmp_eq_u32 s27, 0
	s_cselect_b32 s24, s24, 8736
	s_add_i32 s5, s5, s24
	s_branch .Lcvt_dec
.Lcvt_m3:
	s_cmp_lt_u32 s5, 5040
	s_cbranch_scc1 .Lcvt_dec
	s_add_i32 s5, s5, 3696

.Lcvt_common:
	v_lshlrev_b32_e32 v6, s16, v4
	v_lshl_add_u32 v6, v5, 4, v6
	s_waitcnt lgkmcnt(0)
	s_add_u32 s10, s10, s20
	s_addc_u32 s11, s11, s21
	s_add_i32 s17, s16, 7
	s_lshl_b32 s17, s12, s17
	s_add_u32 s10, s10, s17
	s_addc_u32 s11, s11, 0
	s_lshl_b32 s17, s13, 7
	s_add_u32 s10, s10, s17
	s_addc_u32 s11, s11, 0
	s_add_i32 s17, s16, 3
	s_lshl_b32 s17, 1, s17
	global_load_dwordx4 v[16:19], v6, s[10:11] nt
	s_add_u32 s10, s10, s17
	s_addc_u32 s11, s11, 0
	global_load_dwordx4 v[20:23], v6, s[10:11] nt
	s_add_u32 s10, s10, s17
	s_addc_u32 s11, s11, 0
	global_load_dwordx4 v[24:27], v6, s[10:11] nt
	s_add_u32 s10, s10, s17
	s_addc_u32 s11, s11, 0
	global_load_dwordx4 v[28:31], v6, s[10:11] nt
	s_add_u32 s10, s10, s17
	s_addc_u32 s11, s11, 0
	global_load_dwordx4 v[32:35], v6, s[10:11] nt
	s_add_u32 s10, s10, s17
	s_addc_u32 s11, s11, 0
	global_load_dwordx4 v[36:39], v6, s[10:11] nt
	s_add_u32 s10, s10, s17
	s_addc_u32 s11, s11, 0
	global_load_dwordx4 v[40:43], v6, s[10:11] nt
	s_add_u32 s10, s10, s17
	s_addc_u32 s11, s11, 0
	global_load_dwordx4 v[44:47], v6, s[10:11] nt
	s_add_u32 s10, s10, s17
	s_addc_u32 s11, s11, 0
	global_load_dwordx4 v[48:51], v6, s[10:11] nt
	s_add_u32 s10, s10, s17
	s_addc_u32 s11, s11, 0
	global_load_dwordx4 v[52:55], v6, s[10:11] nt
	s_add_u32 s10, s10, s17
	s_addc_u32 s11, s11, 0
	global_load_dwordx4 v[56:59], v6, s[10:11] nt
	s_add_u32 s10, s10, s17
	s_addc_u32 s11, s11, 0
	global_load_dwordx4 v[60:63], v6, s[10:11] nt
	s_add_u32 s10, s10, s17
	s_addc_u32 s11, s11, 0
	global_load_dwordx4 v[64:67], v6, s[10:11] nt
	s_add_u32 s10, s10, s17
	s_addc_u32 s11, s11, 0
	global_load_dwordx4 v[68:71], v6, s[10:11] nt
	s_add_u32 s10, s10, s17
	s_addc_u32 s11, s11, 0
	global_load_dwordx4 v[72:75], v6, s[10:11] nt
	s_add_u32 s10, s10, s17
	s_addc_u32 s11, s11, 0
	global_load_dwordx4 v[76:79], v6, s[10:11] nt
	s_add_u32 s22, s22, s2
	s_addc_u32 s23, s23, s3
	s_add_u32 s22, s22, s24
	s_addc_u32 s23, s23, 0
	s_lshl_b32 s17, s14, 15
	s_add_u32 s22, s22, s17
	s_addc_u32 s23, s23, 0
	s_lshl_b32 s17, s12, 7
	s_add_u32 s22, s22, s17
	s_addc_u32 s23, s23, 0
	s_mov_b32 s28, 0x0f0f0f0f
	s_mov_b32 s29, 0x0f0f0f0f
	s_mov_b64 exec, s[28:29]
	s_waitcnt vmcnt(15)
	v_mul_f32_e32 v80, 0x42000000, v16
	v_mul_f32_e32 v81, 0x42000000, v17
	v_mul_f32_e32 v82, 0x42000000, v18
	v_mul_f32_e32 v83, 0x42000000, v19
	ds_write_b32 v7, v80 offset:0
	ds_write_b32 v7, v81 offset:4
	ds_write_b32 v7, v82 offset:8
	ds_write_b32 v7, v83 offset:12
	s_waitcnt vmcnt(14)
	v_mul_f32_e32 v80, 0x42000000, v20
	v_mul_f32_e32 v81, 0x42000000, v21
	v_mul_f32_e32 v82, 0x42000000, v22
	v_mul_f32_e32 v83, 0x42000000, v23
	ds_write_b32 v7, v80 offset:544
	ds_write_b32 v7, v81 offset:548
	ds_write_b32 v7, v82 offset:552
	ds_write_b32 v7, v83 offset:556
	s_waitcnt vmcnt(13)
	v_mul_f32_e32 v80, 0x42000000, v24
	v_mul_f32_e32 v81, 0x42000000, v25
	v_mul_f32_e32 v82, 0x42000000, v26
	v_mul_f32_e32 v83, 0x42000000, v27
	ds_write_b32 v7, v80 offset:1088
	ds_write_b32 v7, v81 offset:1092
	ds_write_b32 v7, v82 offset:1096
	ds_write_b32 v7, v83 offset:1100
	s_waitcnt vmcnt(12)
	v_mul_f32_e32 v80, 0x42000000, v28
	v_mul_f32_e32 v81, 0x42000000, v29
	v_mul_f32_e32 v82, 0x42000000, v30
	v_mul_f32_e32 v83, 0x42000000, v31
	ds_write_b32 v7, v80 offset:1632
	ds_write_b32 v7, v81 offset:1636
	ds_write_b32 v7, v82 offset:1640
	ds_write_b32 v7, v83 offset:1644
	s_waitcnt vmcnt(11)
	v_mul_f32_e32 v80, 0x42000000, v32
	v_mul_f32_e32 v81, 0x42000000, v33
	v_mul_f32_e32 v82, 0x42000000, v34
	v_mul_f32_e32 v83, 0x42000000, v35
	ds_write_b32 v7, v80 offset:2176
	ds_write_b32 v7, v81 offset:2180
	ds_write_b32 v7, v82 offset:2184
	ds_write_b32 v7, v83 offset:2188
	s_waitcnt vmcnt(10)
	v_mul_f32_e32 v80, 0x42000000, v36
	v_mul_f32_e32 v81, 0x42000000, v37
	v_mul_f32_e32 v82, 0x42000000, v38
	v_mul_f32_e32 v83, 0x42000000, v39
	ds_write_b32 v7, v80 offset:2720
	ds_write_b32 v7, v81 offset:2724
	ds_write_b32 v7, v82 offset:2728
	ds_write_b32 v7, v83 offset:2732
	s_waitcnt vmcnt(9)
	v_mul_f32_e32 v80, 0x42000000, v40
	v_mul_f32_e32 v81, 0x42000000, v41
	v_mul_f32_e32 v82, 0x42000000, v42
	v_mul_f32_e32 v83, 0x42000000, v43
	ds_write_b32 v7, v80 offset:3264
	ds_write_b32 v7, v81 offset:3268
	ds_write_b32 v7, v82 offset:3272
	ds_write_b32 v7, v83 offset:3276
	s_waitcnt vmcnt(8)
	v_mul_f32_e32 v80, 0x42000000, v44
	v_mul_f32_e32 v81, 0x42000000, v45
	v_mul_f32_e32 v82, 0x42000000, v46
	v_mul_f32_e32 v83, 0x42000000, v47
	ds_write_b32 v7, v80 offset:3808
	ds_write_b32 v7, v81 offset:3812
	ds_write_b32 v7, v82 offset:3816
	ds_write_b32 v7, v83 offset:3820
	s_waitcnt vmcnt(7)
	v_mul_f32_e32 v80, 0x42000000, v48
	v_mul_f32_e32 v81, 0x42000000, v49
	v_mul_f32_e32 v82, 0x42000000, v50
	v_mul_f32_e32 v83, 0x42000000, v51
	ds_write_b32 v7, v80 offset:4352
	ds_write_b32 v7, v81 offset:4356
	ds_write_b32 v7, v82 offset:4360
	ds_write_b32 v7, v83 offset:4364
	s_waitcnt vmcnt(6)
	v_mul_f32_e32 v80, 0x42000000, v52
	v_mul_f32_e32 v81, 0x42000000, v53
	v_mul_f32_e32 v82, 0x42000000, v54
	v_mul_f32_e32 v83, 0x42000000, v55
	ds_write_b32 v7, v80 offset:4896
	ds_write_b32 v7, v81 offset:4900
	ds_write_b32 v7, v82 offset:4904
	ds_write_b32 v7, v83 offset:4908
	s_waitcnt vmcnt(5)
	v_mul_f32_e32 v80, 0x42000000, v56
	v_mul_f32_e32 v81, 0x42000000, v57
	v_mul_f32_e32 v82, 0x42000000, v58
	v_mul_f32_e32 v83, 0x42000000, v59
	ds_write_b32 v7, v80 offset:5440
	ds_write_b32 v7, v81 offset:5444
	ds_write_b32 v7, v82 offset:5448
	ds_write_b32 v7, v83 offset:5452
	s_waitcnt vmcnt(4)
	v_mul_f32_e32 v80, 0x42000000, v60
	v_mul_f32_e32 v81, 0x42000000, v61
	v_mul_f32_e32 v82, 0x42000000, v62
	v_mul_f32_e32 v83, 0x42000000, v63
	ds_write_b32 v7, v80 offset:5984
	ds_write_b32 v7, v81 offset:5988
	ds_write_b32 v7, v82 offset:5992
	ds_write_b32 v7, v83 offset:5996
	s_waitcnt vmcnt(3)
	v_mul_f32_e32 v80, 0x42000000, v64
	v_mul_f32_e32 v81, 0x42000000, v65
	v_mul_f32_e32 v82, 0x42000000, v66
	v_mul_f32_e32 v83, 0x42000000, v67
	ds_write_b32 v7, v80 offset:6528
	ds_write_b32 v7, v81 offset:6532
	ds_write_b32 v7, v82 offset:6536
	ds_write_b32 v7, v83 offset:6540
	s_waitcnt vmcnt(2)
	v_mul_f32_e32 v80, 0x42000000, v68
	v_mul_f32_e32 v81, 0x42000000, v69
	v_mul_f32_e32 v82, 0x42000000, v70
	v_mul_f32_e32 v83, 0x42000000, v71
	ds_write_b32 v7, v80 offset:7072
	ds_write_b32 v7, v81 offset:7076
	ds_write_b32 v7, v82 offset:7080
	ds_write_b32 v7, v83 offset:7084
	s_waitcnt vmcnt(1)
	v_mul_f32_e32 v80, 0x42000000, v72
	v_mul_f32_e32 v81, 0x42000000, v73
	v_mul_f32_e32 v82, 0x42000000, v74
	v_mul_f32_e32 v83, 0x42000000, v75
	ds_write_b32 v7, v80 offset:7616
	ds_write_b32 v7, v81 offset:7620
	ds_write_b32 v7, v82 offset:7624
	ds_write_b32 v7, v83 offset:7628
	s_waitcnt vmcnt(0)
	v_mul_f32_e32 v80, 0x42000000, v76
	v_mul_f32_e32 v81, 0x42000000, v77
	v_mul_f32_e32 v82, 0x42000000, v78
	v_mul_f32_e32 v83, 0x42000000, v79
	ds_write_b32 v7, v80 offset:8160
	ds_write_b32 v7, v81 offset:8164
	ds_write_b32 v7, v82 offset:8168
	ds_write_b32 v7, v83 offset:8172
	s_mov_b64 exec, -1
	s_waitcnt lgkmcnt(0)
	ds_read_b32 v84, v8 offset:0
	ds_read_b32 v85, v8 offset:68
	ds_read_b32 v86, v8 offset:136
	ds_read_b32 v87, v8 offset:204
	ds_read_b32 v88, v8 offset:272
	ds_read_b32 v89, v8 offset:340
	ds_read_b32 v90, v8 offset:408
	ds_read_b32 v91, v8 offset:476
	ds_read_b32 v92, v8 offset:544
	ds_read_b32 v93, v8 offset:612
	ds_read_b32 v94, v8 offset:680
	ds_read_b32 v95, v8 offset:748
	ds_read_b32 v96, v8 offset:816
	ds_read_b32 v97, v8 offset:884
	ds_read_b32 v98, v8 offset:952
	ds_read_b32 v99, v8 offset:1020
	s_waitcnt lgkmcnt(0)
	v_cvt_pk_fp8_f32 v100, v84, v85
	s_nop 0
	v_cvt_pk_fp8_f32 v100, v86, v87 op_sel:[0,0,1]
	v_cvt_pk_fp8_f32 v101, v88, v89
	s_nop 0
	v_cvt_pk_fp8_f32 v101, v90, v91 op_sel:[0,0,1]
	v_cvt_pk_fp8_f32 v102, v92, v93
	s_nop 0
	v_cvt_pk_fp8_f32 v102, v94, v95 op_sel:[0,0,1]
	v_cvt_pk_fp8_f32 v103, v96, v97
	s_nop 0
	v_cvt_pk_fp8_f32 v103, v98, v99 op_sel:[0,0,1]
	s_nop 0
	global_store_dwordx4 v9, v[100:103], s[22:23]
	s_nop 1
	ds_read_b32 v84, v8 offset:32
	ds_read_b32 v85, v8 offset:100
	ds_read_b32 v86, v8 offset:168
	ds_read_b32 v87, v8 offset:236
	ds_read_b32 v88, v8 offset:304
	ds_read_b32 v89, v8 offset:372
	ds_read_b32 v90, v8 offset:440
	ds_read_b32 v91, v8 offset:508
	ds_read_b32 v92, v8 offset:576
	ds_read_b32 v93, v8 offset:644
	ds_read_b32 v94, v8 offset:712
	ds_read_b32 v95, v8 offset:780
	ds_read_b32 v96, v8 offset:848
	ds_read_b32 v97, v8 offset:916
	ds_read_b32 v98, v8 offset:984
	ds_read_b32 v99, v8 offset:1052
	s_waitcnt lgkmcnt(0)
	v_cvt_pk_fp8_f32 v100, v84, v85
	s_nop 0
	v_cvt_pk_fp8_f32 v100, v86, v87 op_sel:[0,0,1]
	v_cvt_pk_fp8_f32 v101, v88, v89
	s_nop 0
	v_cvt_pk_fp8_f32 v101, v90, v91 op_sel:[0,0,1]
	v_cvt_pk_fp8_f32 v102, v92, v93
	s_nop 0
	v_cvt_pk_fp8_f32 v102, v94, v95 op_sel:[0,0,1]
	v_cvt_pk_fp8_f32 v103, v96, v97
	s_nop 0
	v_cvt_pk_fp8_f32 v103, v98, v99 op_sel:[0,0,1]
	s_nop 0
	global_store_dwordx4 v10, v[100:103], s[22:23]
	s_nop 1
	s_waitcnt lgkmcnt(0)
	s_not_b64 s[28:29], s[28:29]
	s_add_u32 s22, s22, 0x4000
	s_addc_u32 s23, s23, 0
	s_mov_b64 exec, s[28:29]
	v_mul_f32_e32 v80, 0x42000000, v16
	v_mul_f32_e32 v81, 0x42000000, v17
	v_mul_f32_e32 v82, 0x42000000, v18
	v_mul_f32_e32 v83, 0x42000000, v19
	ds_write_b32 v7, v80 offset:0
	ds_write_b32 v7, v81 offset:4
	ds_write_b32 v7, v82 offset:8
	ds_write_b32 v7, v83 offset:12
	v_mul_f32_e32 v80, 0x42000000, v20
	v_mul_f32_e32 v81, 0x42000000, v21
	v_mul_f32_e32 v82, 0x42000000, v22
	v_mul_f32_e32 v83, 0x42000000, v23
	ds_write_b32 v7, v80 offset:544
	ds_write_b32 v7, v81 offset:548
	ds_write_b32 v7, v82 offset:552
	ds_write_b32 v7, v83 offset:556
	v_mul_f32_e32 v80, 0x42000000, v24
	v_mul_f32_e32 v81, 0x42000000, v25
	v_mul_f32_e32 v82, 0x42000000, v26
	v_mul_f32_e32 v83, 0x42000000, v27
	ds_write_b32 v7, v80 offset:1088
	ds_write_b32 v7, v81 offset:1092
	ds_write_b32 v7, v82 offset:1096
	ds_write_b32 v7, v83 offset:1100
	v_mul_f32_e32 v80, 0x42000000, v28
	v_mul_f32_e32 v81, 0x42000000, v29
	v_mul_f32_e32 v82, 0x42000000, v30
	v_mul_f32_e32 v83, 0x42000000, v31
	ds_write_b32 v7, v80 offset:1632
	ds_write_b32 v7, v81 offset:1636
	ds_write_b32 v7, v82 offset:1640
	ds_write_b32 v7, v83 offset:1644
	v_mul_f32_e32 v80, 0x42000000, v32
	v_mul_f32_e32 v81, 0x42000000, v33
	v_mul_f32_e32 v82, 0x42000000, v34
	v_mul_f32_e32 v83, 0x42000000, v35
	ds_write_b32 v7, v80 offset:2176
	ds_write_b32 v7, v81 offset:2180
	ds_write_b32 v7, v82 offset:2184
	ds_write_b32 v7, v83 offset:2188
	v_mul_f32_e32 v80, 0x42000000, v36
	v_mul_f32_e32 v81, 0x42000000, v37
	v_mul_f32_e32 v82, 0x42000000, v38
	v_mul_f32_e32 v83, 0x42000000, v39
	ds_write_b32 v7, v80 offset:2720
	ds_write_b32 v7, v81 offset:2724
	ds_write_b32 v7, v82 offset:2728
	ds_write_b32 v7, v83 offset:2732
	v_mul_f32_e32 v80, 0x42000000, v40
	v_mul_f32_e32 v81, 0x42000000, v41
	v_mul_f32_e32 v82, 0x42000000, v42
	v_mul_f32_e32 v83, 0x42000000, v43
	ds_write_b32 v7, v80 offset:3264
	ds_write_b32 v7, v81 offset:3268
	ds_write_b32 v7, v82 offset:3272
	ds_write_b32 v7, v83 offset:3276
	v_mul_f32_e32 v80, 0x42000000, v44
	v_mul_f32_e32 v81, 0x42000000, v45
	v_mul_f32_e32 v82, 0x42000000, v46
	v_mul_f32_e32 v83, 0x42000000, v47
	ds_write_b32 v7, v80 offset:3808
	ds_write_b32 v7, v81 offset:3812
	ds_write_b32 v7, v82 offset:3816
	ds_write_b32 v7, v83 offset:3820
	v_mul_f32_e32 v80, 0x42000000, v48
	v_mul_f32_e32 v81, 0x42000000, v49
	v_mul_f32_e32 v82, 0x42000000, v50
	v_mul_f32_e32 v83, 0x42000000, v51
	ds_write_b32 v7, v80 offset:4352
	ds_write_b32 v7, v81 offset:4356
	ds_write_b32 v7, v82 offset:4360
	ds_write_b32 v7, v83 offset:4364
	v_mul_f32_e32 v80, 0x42000000, v52
	v_mul_f32_e32 v81, 0x42000000, v53
	v_mul_f32_e32 v82, 0x42000000, v54
	v_mul_f32_e32 v83, 0x42000000, v55
	ds_write_b32 v7, v80 offset:4896
	ds_write_b32 v7, v81 offset:4900
	ds_write_b32 v7, v82 offset:4904
	ds_write_b32 v7, v83 offset:4908
	v_mul_f32_e32 v80, 0x42000000, v56
	v_mul_f32_e32 v81, 0x42000000, v57
	v_mul_f32_e32 v82, 0x42000000, v58
	v_mul_f32_e32 v83, 0x42000000, v59
	ds_write_b32 v7, v80 offset:5440
	ds_write_b32 v7, v81 offset:5444
	ds_write_b32 v7, v82 offset:5448
	ds_write_b32 v7, v83 offset:5452
	v_mul_f32_e32 v80, 0x42000000, v60
	v_mul_f32_e32 v81, 0x42000000, v61
	v_mul_f32_e32 v82, 0x42000000, v62
	v_mul_f32_e32 v83, 0x42000000, v63
	ds_write_b32 v7, v80 offset:5984
	ds_write_b32 v7, v81 offset:5988
	ds_write_b32 v7, v82 offset:5992
	ds_write_b32 v7, v83 offset:5996
	v_mul_f32_e32 v80, 0x42000000, v64
	v_mul_f32_e32 v81, 0x42000000, v65
	v_mul_f32_e32 v82, 0x42000000, v66
	v_mul_f32_e32 v83, 0x42000000, v67
	ds_write_b32 v7, v80 offset:6528
	ds_write_b32 v7, v81 offset:6532
	ds_write_b32 v7, v82 offset:6536
	ds_write_b32 v7, v83 offset:6540
	v_mul_f32_e32 v80, 0x42000000, v68
	v_mul_f32_e32 v81, 0x42000000, v69
	v_mul_f32_e32 v82, 0x42000000, v70
	v_mul_f32_e32 v83, 0x42000000, v71
	ds_write_b32 v7, v80 offset:7072
	ds_write_b32 v7, v81 offset:7076
	ds_write_b32 v7, v82 offset:7080
	ds_write_b32 v7, v83 offset:7084
	v_mul_f32_e32 v80, 0x42000000, v72
	v_mul_f32_e32 v81, 0x42000000, v73
	v_mul_f32_e32 v82, 0x42000000, v74
	v_mul_f32_e32 v83, 0x42000000, v75
	ds_write_b32 v7, v80 offset:7616
	ds_write_b32 v7, v81 offset:7620
	ds_write_b32 v7, v82 offset:7624
	ds_write_b32 v7, v83 offset:7628
	v_mul_f32_e32 v80, 0x42000000, v76
	v_mul_f32_e32 v81, 0x42000000, v77
	v_mul_f32_e32 v82, 0x42000000, v78
	v_mul_f32_e32 v83, 0x42000000, v79
	ds_write_b32 v7, v80 offset:8160
	ds_write_b32 v7, v81 offset:8164
	ds_write_b32 v7, v82 offset:8168
	ds_write_b32 v7, v83 offset:8172
	s_mov_b64 exec, -1
	s_waitcnt lgkmcnt(0)
	ds_read_b32 v84, v8 offset:0
	ds_read_b32 v85, v8 offset:68
	ds_read_b32 v86, v8 offset:136
	ds_read_b32 v87, v8 offset:204
	ds_read_b32 v88, v8 offset:272
	ds_read_b32 v89, v8 offset:340
	ds_read_b32 v90, v8 offset:408
	ds_read_b32 v91, v8 offset:476
	ds_read_b32 v92, v8 offset:544
	ds_read_b32 v93, v8 offset:612
	ds_read_b32 v94, v8 offset:680
	ds_read_b32 v95, v8 offset:748
	ds_read_b32 v96, v8 offset:816
	ds_read_b32 v97, v8 offset:884
	ds_read_b32 v98, v8 offset:952
	ds_read_b32 v99, v8 offset:1020
	s_waitcnt lgkmcnt(0)
	v_cvt_pk_fp8_f32 v100, v84, v85
	s_nop 0
	v_cvt_pk_fp8_f32 v100, v86, v87 op_sel:[0,0,1]
	v_cvt_pk_fp8_f32 v101, v88, v89
	s_nop 0
	v_cvt_pk_fp8_f32 v101, v90, v91 op_sel:[0,0,1]
	v_cvt_pk_fp8_f32 v102, v92, v93
	s_nop 0
	v_cvt_pk_fp8_f32 v102, v94, v95 op_sel:[0,0,1]
	v_cvt_pk_fp8_f32 v103, v96, v97
	s_nop 0
	v_cvt_pk_fp8_f32 v103, v98, v99 op_sel:[0,0,1]
	s_nop 0
	global_store_dwordx4 v9, v[100:103], s[22:23]
	s_nop 1
	ds_read_b32 v84, v8 offset:32
	ds_read_b32 v85, v8 offset:100
	ds_read_b32 v86, v8 offset:168
	ds_read_b32 v87, v8 offset:236
	ds_read_b32 v88, v8 offset:304
	ds_read_b32 v89, v8 offset:372
	ds_read_b32 v90, v8 offset:440
	ds_read_b32 v91, v8 offset:508
	ds_read_b32 v92, v8 offset:576
	ds_read_b32 v93, v8 offset:644
	ds_read_b32 v94, v8 offset:712
	ds_read_b32 v95, v8 offset:780
	ds_read_b32 v96, v8 offset:848
	ds_read_b32 v97, v8 offset:916
	ds_read_b32 v98, v8 offset:984
	ds_read_b32 v99, v8 offset:1052
	s_waitcnt lgkmcnt(0)
	v_cvt_pk_fp8_f32 v100, v84, v85
	s_nop 0
	v_cvt_pk_fp8_f32 v100, v86, v87 op_sel:[0,0,1]
	v_cvt_pk_fp8_f32 v101, v88, v89
	s_nop 0
	v_cvt_pk_fp8_f32 v101, v90, v91 op_sel:[0,0,1]
	v_cvt_pk_fp8_f32 v102, v92, v93
	s_nop 0
	v_cvt_pk_fp8_f32 v102, v94, v95 op_sel:[0,0,1]
	v_cvt_pk_fp8_f32 v103, v96, v97
	s_nop 0
	v_cvt_pk_fp8_f32 v103, v98, v99 op_sel:[0,0,1]
	s_nop 0
	global_store_dwordx4 v10, v[100:103], s[22:23]
	s_nop 1
	s_add_i32 s30, s30, s25
	s_add_i32 s26, s26, -1
	s_cmp_lg_u32 s26, 0
	s_cbranch_scc1 .Lcvt_item
